# attn PV epilogue rewritten: address/mask math hoisted before the PV MFMAs, one row address with immediate offsets, four IEEE-division chains interleaved instead of four serial exec-masked blocks
# speedup vs baseline: 1.0157x; 1.0157x over previous
.Lf_pv:
	s_lshr_b32 s2, s49, 4
	s_and_b32 s2, s2, 16
	s_and_b32 s4, s51, 3
	v_and_b32_e32 v62, 15, v0
	v_or_b32_e32 v1, s2, v62
	v_mul_u32_u24_e32 v1, 0x310, v1
	v_and_b32_e32 v50, 48, v0
	s_mov_b32 s6, 0x18000
	v_add3_u32 v1, s6, v1, v50
	s_lshl_b32 s5, s4, 4
	v_or_b32_e32 v51, s5, v62
	v_mul_u32_u24_e32 v51, 0x320, v51
	s_mov_b32 s7, 0x8000
	v_add3_u32 v51, s7, v51, v50
	v_mov_b32_e32 v74, 0x3c003c00
	v_mov_b32_e32 v75, v74
	v_mov_b32_e32 v76, v74
	v_mov_b32_e32 v77, v74
	ds_read_b128 v[2:5], v1
	ds_read_b128 v[102:105], v51
	ds_read_b128 v[6:9], v1 offset:64
	ds_read_b128 v[106:109], v51 offset:64
	ds_read_b128 v[10:13], v1 offset:128
	ds_read_b128 v[110:113], v51 offset:128
	ds_read_b128 v[14:17], v1 offset:192
	ds_read_b128 v[114:117], v51 offset:192
	ds_read_b128 v[18:21], v1 offset:256
	ds_read_b128 v[118:121], v51 offset:256
	ds_read_b128 v[22:25], v1 offset:320
	ds_read_b128 v[122:125], v51 offset:320
	ds_read_b128 v[26:29], v1 offset:384
	ds_read_b128 v[126:129], v51 offset:384
	s_lshr_b32 s3, s43, 3
	s_mul_i32 s5, s3, 0x180
	s_add_i32 s5, s5, s41
	v_lshrrev_b32_e32 v78, 2, v0
	v_and_or_b32 v78, v78, 12, s2
	s_lshl_b32 s2, s33, 7
	s_and_b32 s2, s2, 0x380
	s_add_u32 s0, s62, s2
	s_addc_u32 s1, s63, 0
	s_lshl_b32 s2, s4, 5
	s_add_u32 s0, s0, s2
	s_addc_u32 s1, s1, 0
	v_add_u32_e32 v80, s5, v78
	v_mov_b32_e32 v81, 0
	v_lshlrev_b64 v[80:81], 10, v[80:81]
	v_lshlrev_b32_e32 v82, 1, v62
	v_mov_b32_e32 v83, 0
	v_lshl_add_u64 v[80:81], v[80:81], 0, v[82:83]
	v_lshl_add_u64 v[80:81], s[0:1], 0, v[80:81]
	s_waitcnt lgkmcnt(12)
	v_mfma_f32_16x16x32_f16 v[66:69], v[2:5], v[102:105], 0
	v_mfma_f32_16x16x32_f16 v[70:73], v[2:5], v[74:77], 0
	ds_read_b128 v[30:33], v1 offset:448
	ds_read_b128 v[130:133], v51 offset:448
	s_waitcnt lgkmcnt(12)
	v_mfma_f32_16x16x32_f16 v[66:69], v[6:9], v[106:109], v[66:69]
	v_mfma_f32_16x16x32_f16 v[70:73], v[6:9], v[74:77], v[70:73]
	ds_read_b128 v[34:37], v1 offset:512
	ds_read_b128 v[134:137], v51 offset:512
	s_waitcnt lgkmcnt(12)
	v_mfma_f32_16x16x32_f16 v[66:69], v[10:13], v[110:113], v[66:69]
	v_mfma_f32_16x16x32_f16 v[70:73], v[10:13], v[74:77], v[70:73]
	ds_read_b128 v[38:41], v1 offset:576
	ds_read_b128 v[138:141], v51 offset:576
	s_waitcnt lgkmcnt(12)
	v_mfma_f32_16x16x32_f16 v[66:69], v[14:17], v[114:117], v[66:69]
	v_mfma_f32_16x16x32_f16 v[70:73], v[14:17], v[74:77], v[70:73]
	ds_read_b128 v[42:45], v1 offset:640
	ds_read_b128 v[142:145], v51 offset:640
	s_waitcnt lgkmcnt(12)
	v_mfma_f32_16x16x32_f16 v[66:69], v[18:21], v[118:121], v[66:69]
	v_mfma_f32_16x16x32_f16 v[70:73], v[18:21], v[74:77], v[70:73]
	ds_read_b128 v[46:49], v1 offset:704
	ds_read_b128 v[146:149], v51 offset:704
	s_waitcnt lgkmcnt(12)
	v_mfma_f32_16x16x32_f16 v[66:69], v[22:25], v[122:125], v[66:69]
	v_mfma_f32_16x16x32_f16 v[70:73], v[22:25], v[74:77], v[70:73]
	s_waitcnt lgkmcnt(10)
	v_mfma_f32_16x16x32_f16 v[66:69], v[26:29], v[126:129], v[66:69]
	v_mfma_f32_16x16x32_f16 v[70:73], v[26:29], v[74:77], v[70:73]
	s_waitcnt lgkmcnt(8)
	v_mfma_f32_16x16x32_f16 v[66:69], v[30:33], v[130:133], v[66:69]
	v_mfma_f32_16x16x32_f16 v[70:73], v[30:33], v[74:77], v[70:73]
	s_waitcnt lgkmcnt(6)
	v_mfma_f32_16x16x32_f16 v[66:69], v[34:37], v[134:137], v[66:69]
	v_mfma_f32_16x16x32_f16 v[70:73], v[34:37], v[74:77], v[70:73]
	s_waitcnt lgkmcnt(4)
	v_mfma_f32_16x16x32_f16 v[66:69], v[38:41], v[138:141], v[66:69]
	v_mfma_f32_16x16x32_f16 v[70:73], v[38:41], v[74:77], v[70:73]
	s_waitcnt lgkmcnt(2)
	v_mfma_f32_16x16x32_f16 v[66:69], v[42:45], v[142:145], v[66:69]
	v_mfma_f32_16x16x32_f16 v[70:73], v[42:45], v[74:77], v[70:73]
	s_waitcnt lgkmcnt(0)
	v_mfma_f32_16x16x32_f16 v[66:69], v[46:49], v[146:149], v[66:69]
	v_mfma_f32_16x16x32_f16 v[70:73], v[46:49], v[74:77], v[70:73]
	v_cmp_gt_u32_e64 s[0:1], 24, v78
	s_nop 7
	v_div_scale_f32 v84, s[6:7], v70, v70, 1.0
	v_div_scale_f32 v85, s[6:7], v71, v71, 1.0
	v_div_scale_f32 v86, s[6:7], v72, v72, 1.0
	v_div_scale_f32 v87, s[6:7], v73, v73, 1.0
	v_rcp_f32_e32 v88, v84
	v_rcp_f32_e32 v89, v85
	v_rcp_f32_e32 v90, v86
	v_rcp_f32_e32 v91, v87
	v_div_scale_f32 v92, s[10:11], 1.0, v70, 1.0
	v_div_scale_f32 v93, s[12:13], 1.0, v71, 1.0
	v_div_scale_f32 v94, s[14:15], 1.0, v72, 1.0
	v_div_scale_f32 v95, s[16:17], 1.0, v73, 1.0
	v_fma_f32 v96, -v84, v88, 1.0
	v_fma_f32 v97, -v85, v89, 1.0
	v_fma_f32 v98, -v86, v90, 1.0
	v_fma_f32 v99, -v87, v91, 1.0
	v_fmac_f32_e32 v88, v96, v88
	v_fmac_f32_e32 v89, v97, v89
	v_fmac_f32_e32 v90, v98, v90
	v_fmac_f32_e32 v91, v99, v91
	v_mul_f32_e32 v100, v92, v88
	v_mul_f32_e32 v101, v93, v89
	v_mul_f32_e32 v102, v94, v90
	v_mul_f32_e32 v103, v95, v91
	v_fma_f32 v96, -v84, v100, v92
	v_fma_f32 v97, -v85, v101, v93
	v_fma_f32 v98, -v86, v102, v94
	v_fma_f32 v99, -v87, v103, v95
	v_fmac_f32_e32 v100, v96, v88
	v_fmac_f32_e32 v101, v97, v89
	v_fmac_f32_e32 v102, v98, v90
	v_fmac_f32_e32 v103, v99, v91
	v_fma_f32 v84, -v84, v100, v92
	v_fma_f32 v85, -v85, v101, v93
	v_fma_f32 v86, -v86, v102, v94
	v_fma_f32 v87, -v87, v103, v95
	s_mov_b64 vcc, s[10:11]
	s_nop 3
	v_div_fmas_f32 v84, v84, v88, v100
	s_mov_b64 vcc, s[12:13]
	s_nop 3
	v_div_fmas_f32 v85, v85, v89, v101
	s_mov_b64 vcc, s[14:15]
	s_nop 3
	v_div_fmas_f32 v86, v86, v90, v102
	s_mov_b64 vcc, s[16:17]
	s_nop 3
	v_div_fmas_f32 v87, v87, v91, v103
	v_div_fixup_f32 v84, v84, v70, 1.0
	v_div_fixup_f32 v85, v85, v71, 1.0
	v_div_fixup_f32 v86, v86, v72, 1.0
	v_div_fixup_f32 v87, v87, v73, 1.0
	v_fma_mixlo_f16 v66, v66, v84, 0
	v_fma_mixlo_f16 v67, v67, v85, 0
	v_fma_mixlo_f16 v68, v68, v86, 0
	v_fma_mixlo_f16 v69, v69, v87, 0
	s_and_saveexec_b64 s[2:3], s[0:1]
	global_store_short v[80:81], v66, off
	global_store_short v[80:81], v67, off offset:1024
	global_store_short v[80:81], v68, off offset:2048
	global_store_short v[80:81], v69, off offset:3072
	s_endpgm
